# speedup vs baseline: 1.0015x; 1.0015x over previous
_Z12final_kernelPKfS0_Pfi:
	s_load_dwordx2 s[2:3], s[0:1], 0x8
	s_load_dwordx2 s[14:15], s[0:1], 0x0
	s_load_dwordx2 s[16:17], s[0:1], 0x10
	v_and_b32_e32 v35, 63, v0
	v_lshlrev_b32_e32 v35, 2, v35
	v_lshlrev_b32_e32 v1, 4, v0
	v_or_b32_e32 v34, 0x400, v0
	v_or_b32_e32 v33, 0x800, v0
	v_lshlrev_b32_e32 v2, 4, v34
	s_waitcnt lgkmcnt(0)
	global_load_dword v35, v35, s[14:15]
	global_load_dwordx4 v[26:29], v1, s[2:3]
	global_load_dwordx4 v[22:25], v2, s[2:3]
	v_lshlrev_b32_e32 v1, 4, v33
	v_or_b32_e32 v32, 0xc00, v0
	v_or_b32_e32 v31, 0x1000, v0
	v_lshlrev_b32_e32 v2, 4, v32
	global_load_dwordx4 v[18:21], v1, s[2:3]
	global_load_dwordx4 v[14:17], v2, s[2:3]
	v_lshlrev_b32_e32 v1, 4, v31
	v_or_b32_e32 v30, 0x1400, v0
	v_lshlrev_b32_e32 v2, 4, v30
	global_load_dwordx4 v[10:13], v1, s[2:3]
	global_load_dwordx4 v[6:9], v2, s[2:3]
	v_or_b32_e32 v1, 0x1800, v0
	s_movk_i32 s4, 0x1940
	v_cmp_gt_u32_e32 vcc, s4, v1
	s_and_saveexec_b64 s[4:5], vcc
	s_cbranch_execz .LBB1_2
	v_lshlrev_b32_e32 v2, 4, v1
	global_load_dwordx4 v[2:5], v2, s[2:3]

.LBB1_4:
	s_or_b64 exec, exec, s[4:5]
	v_cmp_eq_u32_e32 vcc, 0, v0
	s_and_saveexec_b64 s[2:3], vcc
	v_mov_b32_e32 v1, 0x64
	v_mov_b32_e32 v2, 0
	ds_write_b32 v2, v1 offset:26112
	s_or_b64 exec, exec, s[2:3]
	v_cmp_gt_u32_e32 vcc, 64, v0
	v_lshlrev_b32_e32 v2, 2, v0
	s_waitcnt lgkmcnt(0)
	s_barrier
	s_and_saveexec_b64 s[2:3], vcc
	s_cbranch_execz .LBB1_8
	v_mul_u32_u24_e32 v3, 0x194, v0
	ds_read_b32 v3, v3 offset:400
	s_waitcnt vmcnt(0) lgkmcnt(0)
	v_mul_f32_e32 v1, v35, v3
	ds_write_b32 v2, v1 offset:25856
.LBB1_8:
	s_or_b64 exec, exec, s[2:3]
	s_mov_b64 s[4:5], s[16:17]
	s_movk_i32 s2, 0x320
	v_cmp_gt_u32_e32 vcc, s2, v0
	s_waitcnt lgkmcnt(0)
	s_barrier
	s_and_saveexec_b64 s[6:7], vcc
	s_cbranch_execz .LBB1_14
	v_and_b32_e32 v3, 7, v0
	v_lshrrev_b32_e32 v1, 3, v0
	v_mul_u32_u24_e32 v4, 0xca0, v3
	v_lshl_add_u32 v8, v1, 2, v4
	ds_read2_b32 v[12:13], v8 offset1:101
	v_lshlrev_b32_e32 v9, 5, v3
	v_add_u32_e32 v4, 0x200, v8
	ds_read2_b32 v[14:15], v4 offset0:74 offset1:175
	v_add_u32_e32 v10, 0x400, v8
	ds_read_b128 v[4:7], v9 offset:25856
	ds_read2_b32 v[16:17], v10 offset0:148 offset1:249
	v_add_u32_e32 v8, 0x800, v8
	ds_read2_b32 v[18:19], v8 offset0:94 offset1:195
	ds_read_b128 v[8:11], v9 offset:25872
	s_movk_i32 s2, 0xff
	s_waitcnt lgkmcnt(3)
	v_cmp_nlt_f32_e32 vcc, v13, v5
	s_nop 1
	v_cndmask_b32_e64 v5, 0, 1, vcc
	v_cmp_nlt_f32_e32 vcc, v12, v4
	v_lshlrev_b16_e32 v5, 1, v5
	s_nop 0
	v_cndmask_b32_e64 v4, 0, 1, vcc
	v_cmp_nlt_f32_e32 vcc, v14, v6
	v_bitop3_b16 v4, v4, 3, v5 bitop3:0xc8
	s_nop 0
	v_cndmask_b32_e64 v5, 0, 1, vcc
	v_cmp_nlt_f32_e32 vcc, v15, v7
	v_lshlrev_b16_e32 v5, 2, v5
	s_nop 0
	v_cndmask_b32_e64 v6, 0, 1, vcc
	v_lshlrev_b16_e32 v6, 3, v6
	v_or_b32_e32 v5, v6, v5
	s_waitcnt lgkmcnt(0)
	v_cmp_nlt_f32_e32 vcc, v18, v10
	v_bitop3_b16 v4, v4, 15, v5 bitop3:0xc8
	s_nop 0
	v_cndmask_b32_e64 v5, 0, 1, vcc
	v_cmp_nlt_f32_e32 vcc, v19, v11
	v_lshlrev_b16_e32 v5, 2, v5
	s_nop 0
	v_cndmask_b32_e64 v6, 0, 1, vcc
	v_lshlrev_b16_e32 v6, 3, v6
	v_cmp_nlt_f32_e32 vcc, v17, v9
	v_or_b32_e32 v5, v6, v5
	s_nop 0
	v_cndmask_b32_e64 v6, 0, 1, vcc
	v_cmp_nlt_f32_e32 vcc, v16, v8
	v_lshlrev_b16_e32 v6, 1, v6
	s_nop 0
	v_cndmask_b32_e64 v7, 0, 1, vcc
	v_or_b32_e32 v6, v7, v6
	v_bitop3_b16 v5, v6, v5, 3 bitop3:0xec
	v_lshlrev_b16_e32 v5, 4, v5
	v_bitop3_b16 v4, v4, s2, v5 bitop3:0xc8
	v_mbcnt_lo_u32_b32 v5, -1, 0
	v_mbcnt_hi_u32_b32 v5, -1, v5
	v_and_b32_e32 v7, 64, v5
	v_cmp_eq_u16_e32 vcc, 0, v4
	v_xor_b32_e32 v6, 1, v5
	v_add_u32_e32 v7, 64, v7
	v_cndmask_b32_e64 v4, 0, 1, vcc
	v_cmp_lt_i32_e32 vcc, v6, v7
	v_xor_b32_e32 v9, 2, v5
	s_nop 0
	v_cndmask_b32_e32 v6, v5, v6, vcc
	v_lshlrev_b32_e32 v6, 2, v6
	ds_bpermute_b32 v6, v6, v4
	v_cmp_lt_i32_e32 vcc, v9, v7
	s_waitcnt lgkmcnt(0)
	v_and_b32_e32 v8, v6, v4
	v_cndmask_b32_e32 v9, v5, v9, vcc
	v_lshlrev_b32_e32 v9, 2, v9
	ds_bpermute_b32 v9, v9, v8
	s_waitcnt lgkmcnt(0)
	v_bitop3_b32 v4, v6, v9, v4 bitop3:0x80
	v_xor_b32_e32 v6, 4, v5
	v_cmp_lt_i32_e32 vcc, v6, v7
	s_nop 1
	v_cndmask_b32_e32 v5, v5, v6, vcc
	v_lshlrev_b32_e32 v5, 2, v5
	ds_bpermute_b32 v4, v5, v4
	v_cmp_eq_u32_e32 vcc, 0, v3
	s_waitcnt lgkmcnt(0)
	v_bitop3_b32 v4, v8, v4, v9 bitop3:0x80
	v_and_b32_e32 v3, 1, v4
	v_cmp_eq_u32_e64 s[2:3], 1, v3
	s_and_b64 s[2:3], vcc, s[2:3]
	s_and_b64 exec, exec, s[2:3]
	s_cbranch_execz .LBB1_14
	s_mov_b64 s[2:3], exec
	s_brev_b32 s8, -2

	.amdhsa_kernel _Z12final_kernelPKfS0_Pfi
		.amdhsa_group_segment_fixed_size 26116
		.amdhsa_private_segment_fixed_size 0
		.amdhsa_kernarg_size 28
		.amdhsa_user_sgpr_count 2
		.amdhsa_user_sgpr_dispatch_ptr 0
		.amdhsa_user_sgpr_queue_ptr 0
		.amdhsa_user_sgpr_kernarg_segment_ptr 1
		.amdhsa_user_sgpr_dispatch_id 0
		.amdhsa_user_sgpr_kernarg_preload_length 0
		.amdhsa_user_sgpr_kernarg_preload_offset 0
		.amdhsa_user_sgpr_private_segment_size 0
		.amdhsa_uses_dynamic_stack 0
		.amdhsa_enable_private_segment 0
		.amdhsa_system_sgpr_workgroup_id_x 1
		.amdhsa_system_sgpr_workgroup_id_y 0
		.amdhsa_system_sgpr_workgroup_id_z 0
		.amdhsa_system_sgpr_workgroup_info 0
		.amdhsa_system_vgpr_workitem_id 0
		.amdhsa_next_free_vgpr 36
		.amdhsa_next_free_sgpr 18
		.amdhsa_accum_offset 36
		.amdhsa_reserve_vcc 1
		.amdhsa_float_round_mode_32 0
		.amdhsa_float_round_mode_16_64 0
		.amdhsa_float_denorm_mode_32 3
		.amdhsa_float_denorm_mode_16_64 3
		.amdhsa_dx10_clamp 1
		.amdhsa_ieee_mode 1
		.amdhsa_fp16_overflow 0
		.amdhsa_tg_split 0
		.amdhsa_exception_fp_ieee_invalid_op 0
		.amdhsa_exception_fp_denorm_src 0
		.amdhsa_exception_fp_ieee_div_zero 0
		.amdhsa_exception_fp_ieee_overflow 0
		.amdhsa_exception_fp_ieee_underflow 0
		.amdhsa_exception_fp_ieee_inexact 0
		.amdhsa_exception_int_div_zero 0
	.end_amdhsa_kernel

amdhsa.kernels:
  - .agpr_count:     240
    .args:
      - .actual_access:  read_only
        .address_space:  global
        .offset:         0
        .size:           8
        .value_kind:     global_buffer
      - .actual_access:  read_only
        .address_space:  global
        .offset:         8
        .size:           8
        .value_kind:     global_buffer
      - .actual_access:  read_only
        .address_space:  global
        .offset:         16
        .size:           8
        .value_kind:     global_buffer
      - .address_space:  global
        .offset:         24
        .size:           8
        .value_kind:     global_buffer
      - .actual_access:  write_only
        .address_space:  global
        .offset:         32
        .size:           8
        .value_kind:     global_buffer
    .group_segment_fixed_size: 158272
    .kernarg_segment_align: 8
    .kernarg_segment_size: 40
    .language:       OpenCL C
    .language_version:
      - 2
      - 0
    .max_flat_workgroup_size: 256
    .name:           _Z11jacobi_mainPKfS0_S0_PyPf
    .private_segment_fixed_size: 0
    .sgpr_count:     80
    .sgpr_spill_count: 0
    .symbol:         _Z11jacobi_mainPKfS0_S0_PyPf.kd
    .uniform_work_group_size: 1
    .uses_dynamic_stack: false
    .vgpr_count:     496
    .vgpr_spill_count: 0
    .wavefront_size: 64
  - .agpr_count:     0
    .args:
      - .actual_access:  read_only
        .address_space:  global
        .offset:         0
        .size:           8
        .value_kind:     global_buffer
      - .actual_access:  read_only
        .address_space:  global
        .offset:         8
        .size:           8
        .value_kind:     global_buffer
      - .actual_access:  write_only
        .address_space:  global
        .offset:         16
        .size:           8
        .value_kind:     global_buffer
      - .offset:         24
        .size:           4
        .value_kind:     by_value
    .group_segment_fixed_size: 26116
    .kernarg_segment_align: 8
    .kernarg_segment_size: 28
    .language:       OpenCL C
    .language_version:
      - 2
      - 0
    .max_flat_workgroup_size: 1024
    .name:           _Z12final_kernelPKfS0_Pfi
    .private_segment_fixed_size: 0
    .sgpr_count:     24
    .sgpr_spill_count: 0
    .symbol:         _Z12final_kernelPKfS0_Pfi.kd
    .uniform_work_group_size: 1
    .uses_dynamic_stack: false
    .vgpr_count:     36
    .vgpr_spill_count: 0
    .wavefront_size: 64
